# lru_local MFMA chains start from inline 0; in-proj gate clamp without the redundant canonicalize; attention-prep rows rebalanced (6/114 instead of 18/110)
# speedup vs baseline: 1.0042x; 1.0042x over previous
.LBB0_63:
	s_or_b64 exec, exec, s[30:31]
	v_readlane_b32 s28, v251, 0
	s_lshl_b32 s33, s28, 9
	s_add_u32 s60, s92, 0x5fb21b00
	s_addc_u32 s61, s93, 0
	s_lshl_b32 s89, s28, 3
	s_add_u32 s0, s92, 0x3600
	s_addc_u32 s1, s93, 0
	s_add_u32 s86, s92, 0x37bddb00
	s_addc_u32 s87, s93, 0
	s_add_u32 s96, s92, 0x37abdb00
	v_writelane_b32 v251, s0, 51
	s_addc_u32 s97, s93, 0
	s_movk_i32 s3, 0xfd
	v_writelane_b32 v251, s1, 52
	s_add_u32 s0, s92, 0x4803600
	s_addc_u32 s1, s93, 0
	v_writelane_b32 v251, s0, 53
	s_mul_i32 s9, s28, 0x72
	s_mul_i32 s10, s28, 6
	v_writelane_b32 v251, s1, 54
	s_add_u32 s0, s92, 0x40d21b00
	s_addc_u32 s1, s93, 0
	s_add_u32 s90, s92, 0x48db600
	v_writelane_b32 v251, s0, 55
	s_addc_u32 s91, s93, 0
	v_mov_b32_e32 v131, 0
	v_writelane_b32 v251, s1, 56
	s_add_u32 s0, s92, 0x4e821b00
	v_writelane_b32 v251, s0, 57
	s_addc_u32 s0, s93, 0
	v_writelane_b32 v251, s0, 58
	s_add_u32 s0, s92, 0x46821b00
	v_writelane_b32 v251, s0, 59
	s_addc_u32 s0, s93, 0
	v_writelane_b32 v251, s0, 60
	s_add_u32 s0, s92, 0x46621b00
	v_writelane_b32 v251, s0, 61
	s_addc_u32 s0, s93, 0
	v_writelane_b32 v251, s0, 62
	s_add_u32 s0, s92, 0x46321b00
	v_writelane_b32 v251, s0, 63
	s_addc_u32 s0, s93, 0
	v_writelane_b32 v252, s0, 0
	s_add_u32 s0, s92, 0x45521b00
	v_writelane_b32 v252, s0, 1
	s_addc_u32 s0, s93, 0
	v_writelane_b32 v252, s0, 2
	s_add_u32 s0, s92, 0x6cdb600
	s_addc_u32 s1, s93, 0
	v_writelane_b32 v252, s0, 3
	s_cmpk_lt_i32 s28, 0x7e0
	v_mov_b32_e32 v1, 0x358637bd
	v_writelane_b32 v252, s1, 4
	s_cselect_b64 s[0:1], -1, 0
	v_writelane_b32 v252, s0, 5
	s_ashr_i32 s29, s28, 31
	v_writelane_b32 v254, s29, 0
	v_writelane_b32 v252, s1, 6
	s_lshr_b32 s0, s29, 29
	s_add_i32 s0, s28, s0
	s_ashr_i32 s30, s0, 3
	s_and_b32 s0, s0, -8
	s_sub_i32 s31, s28, s0
	s_lshl_b32 s2, s31, 5
	s_cmp_lt_i32 s31, 0
	s_cselect_b64 s[0:1], -1, 0
	v_writelane_b32 v252, s0, 7
	v_mov_b32_e32 v226, 1
	v_mov_b32_e32 v227, 0x3ecc95a3
	v_writelane_b32 v252, s1, 8
	s_and_b64 s[0:1], s[0:1], exec
	s_cselect_b32 s0, s3, 0xfc
	s_mul_i32 s0, s0, s31
	s_mul_i32 s1, s31, 33
	s_cselect_b32 s8, s1, s2
	s_add_i32 s0, s0, s30
	s_mul_hi_i32 s1, s0, 0x92492493
	s_add_i32 s1, s1, s0
	s_lshr_b32 s2, s1, 31
	s_ashr_i32 s1, s1, 7
	s_add_i32 s1, s1, s2
	s_mul_i32 s2, s1, 0xe0
	s_sub_i32 s2, s0, s2
	s_bfe_u32 s0, s2, 0x3001c
	s_add_i32 s3, s2, s0
	s_sext_i32_i16 s4, s3
	s_and_b32 s3, s3, 0xfff8
	s_sub_i32 s2, s2, s3
	s_lshl_b32 s1, s1, 3
	s_sext_i32_i16 s2, s2
	s_add_i32 s6, s1, s2
	s_ashr_i32 s1, s4, 3
	v_writelane_b32 v252, s1, 9
	s_mov_b32 s2, s6
	s_ashr_i32 s7, s6, 31
	v_writelane_b32 v252, s2, 10
	s_lshr_b32 s0, s4, 3
	v_mov_b32_e32 v228, 0x3c088889
	v_writelane_b32 v252, s3, 11
	s_lshl_b64 s[2:3], s[6:7], 19
	s_add_u32 s34, s90, s2
	s_addc_u32 s35, s91, s3
	s_bfe_i64 s[0:1], s[0:1], 0x100000
	s_lshl_b64 s[0:1], s[0:1], 19
	v_writelane_b32 v252, s0, 12
	s_cmpk_lt_i32 s28, 0x480
	v_mov_b32_e32 v241, 0xfdac0000
	v_writelane_b32 v252, s1, 13
	s_cselect_b64 s[0:1], -1, 0
	v_writelane_b32 v252, s0, 14
	v_mov_b32_e32 v250, 0xffffc980
	v_mov_b32_e32 v229, 0x80
	v_writelane_b32 v252, s1, 15
	s_add_u32 s0, s92, 0x168db600
	s_addc_u32 s1, s93, 0
	s_add_u32 s11, s92, 0x1e6db600
	s_addc_u32 s12, s93, 0
	s_add_u32 s14, s92, 0x22edb600
	s_addc_u32 s15, s93, 0
	v_writelane_b32 v252, s0, 16
	s_cmpk_gt_i32 s28, 0x7f
	v_mov_b32_e32 v232, 0x100
	v_writelane_b32 v252, s1, 17
	s_cselect_b64 s[0:1], -1, 0
	v_writelane_b32 v252, s0, 18
	s_addk_i32 s9, 0xd600
	s_addk_i32 s10, 0x1980
	v_writelane_b32 v252, s1, 19
	s_add_u32 s0, s92, 0x276ddb00
	s_addc_u32 s1, s93, 0
	v_writelane_b32 v252, s0, 20
	v_mov_b32_e32 v233, 0x41f00000
	v_mov_b32_e32 v234, 0x7f800000
	v_writelane_b32 v252, s1, 21
	s_and_b32 s0, s28, 0xffffffe0
	s_add_i32 s1, s28, 0x80
	s_cmpk_eq_i32 s0, 0x80
	s_cselect_b32 s0, s1, -1
	v_writelane_b32 v252, s0, 22
	s_add_u32 s0, s92, 0x28d5db00
	s_addc_u32 s1, s93, 0
	v_writelane_b32 v252, s0, 23
	v_mov_b32_e32 v192, 0x3f317218
	v_mov_b32_e32 v235, 0x44
	v_writelane_b32 v252, s1, 24
	s_add_u32 s0, s92, 0x31d5db00
	s_addc_u32 s1, s93, 0
	v_writelane_b32 v252, s0, 25
	v_mov_b32_e32 v240, 0xf149f2ca
	v_mov_b64_e32 v[194:195], 0x100
	v_writelane_b32 v252, s1, 26
	s_add_u32 s0, s92, 0x31e7db00
	s_addc_u32 s1, s93, 0
	v_writelane_b32 v252, s0, 27
	v_mov_b64_e32 v[196:197], 0xff
	s_movk_i32 s88, 0x4000
	v_writelane_b32 v252, s1, 28
	s_add_i32 s0, s28, 0xffffff80
	v_writelane_b32 v252, s0, 29
	s_add_u32 s0, s92, 0x288ddb00
	s_addc_u32 s1, s93, 0
	v_writelane_b32 v252, s0, 30
	s_mov_b32 s77, 0x8000
	s_mov_b32 s82, 0xc000
	v_writelane_b32 v252, s1, 31
	s_sub_i32 s0, 0xff, s28
	s_ashr_i32 s1, s0, 31
	s_lshl_b64 s[0:1], s[0:1], 9
	v_writelane_b32 v252, s0, 32
	s_mov_b32 s80, 0x10000
	s_mov_b32 s83, 0x18000
	v_writelane_b32 v252, s1, 33
	s_add_u32 s0, s92, 0x31f9db00
	s_addc_u32 s1, s93, 0
	v_writelane_b32 v252, s0, 34
	s_movk_i32 s76, 0x2000
	s_movk_i32 s75, 0x6000
	v_writelane_b32 v252, s1, 35
	s_mul_i32 s0, s30, 0xffffff81
	s_lshl_b32 s1, s28, 4
	s_add_i32 s1, s0, s1
	s_ashr_i32 s2, s1, 2
	s_lshr_b32 s3, s2, 30
	s_add_i32 s3, s2, s3
	s_and_b32 s3, s3, -4
	s_sub_i32 s4, s2, s3
	s_ashr_i32 s2, s1, 31
	s_lshr_b32 s2, s2, 28
	s_add_i32 s1, s1, s2
	s_bfe_i32 s2, s0, 0x10001
	s_bfe_u32 s5, s0, 0x10001
	s_lshl_b32 s0, s30, 1
	s_ashr_i32 s6, s1, 4
	s_and_b32 s0, s0, 2
	v_writelane_b32 v252, s0, 36
	s_lshl_b32 s0, s6, 2
	s_add_i32 s1, s0, 0x100
	s_cmp_eq_u32 s5, 0
	s_cselect_b64 s[16:17], -1, 0
	s_and_b32 s0, s2, 3
	s_or_b32 s0, s1, s0
	s_lshl_b32 s0, s0, 3
	s_lshl_b32 s7, s4, 1
	s_add_i32 s0, s0, s7
	s_or_b32 s2, s0, s5
	s_ashr_i32 s3, s2, 31
	v_writelane_b32 v252, s1, 37
	s_lshl_b64 s[0:1], s[2:3], 15
	v_writelane_b32 v252, s11, 38
	s_add_u32 s0, s11, s0
	v_writelane_b32 v252, s0, 39
	v_writelane_b32 v252, s12, 40
	s_addc_u32 s0, s12, s1
	v_writelane_b32 v252, s0, 41
	s_lshl_b64 s[0:1], s[2:3], 2
	s_add_u32 s0, s14, s0
	v_writelane_b32 v252, s14, 42
	s_addc_u32 s1, s15, s1
	s_movk_i32 s3, 0x200
	v_writelane_b32 v252, s15, 43
	v_writelane_b32 v252, s0, 44
	s_movk_i32 s54, 0x1000
	s_movk_i32 s81, 0x3800
	v_writelane_b32 v252, s1, 45
	s_or_b32 s0, s7, s5
	v_writelane_b32 v252, s0, 46
	s_lshl_b32 s0, s6, 5
	v_writelane_b32 v252, s0, 47
	s_and_b64 s[0:1], s[16:17], exec
	s_movk_i32 s0, 0x800
	s_cselect_b32 s0, s0, 0xfffff800
	s_mulk_i32 s5, 0x4800
	v_writelane_b32 v252, s0, 48
	s_cselect_b32 s0, 0, 63
	s_or_b32 s0, s0, s5
	v_writelane_b32 v252, s0, 49
	s_lshl_b32 s0, s4, 7
	s_ashr_i32 s1, s0, 31
	v_writelane_b32 v252, s16, 50
	s_and_b64 s[4:5], s[16:17], exec
	s_cselect_b32 s36, s3, 0xfffffe00
	s_cselect_b32 s37, 0, -1
	s_add_u32 s4, s92, 0x22eddb00
	s_addc_u32 s5, s93, 0
	s_lshl_b64 s[0:1], s[0:1], 1
	v_writelane_b32 v252, s17, 51
	s_add_u32 s0, s4, s0
	v_writelane_b32 v252, s0, 52
	v_writelane_b32 v252, s4, 53
	s_addc_u32 s0, s5, s1
	s_add_u32 s38, s92, 0x320bdb00
	s_addc_u32 s39, s93, 0
	s_add_u32 s40, s92, 0x356bdb00
	v_writelane_b32 v252, s5, 54
	s_addc_u32 s41, s93, 0
	v_writelane_b32 v252, s0, 55
	s_cmpk_lt_i32 s28, 0x100
	s_mul_hi_i32 s0, s28, 0x2aaaaaab
	s_cselect_b64 s[4:5], -1, 0
	s_lshr_b32 s1, s0, 31
	s_add_i32 s3, s0, s1
	s_ashr_i32 s0, s0, 2
	s_add_i32 s11, s0, s1
	s_ashr_i32 s0, s3, 31
	s_lshr_b32 s0, s0, 30
	s_add_i32 s0, s3, s0
	s_and_b32 s0, s0, -4
	s_mul_i32 s1, s3, 6
	s_sub_i32 s12, s3, s0
	s_sub_i32 s0, s28, s1
	s_ashr_i32 s6, s0, 1
	v_writelane_b32 v252, s4, 56
	s_ashr_i32 s7, s6, 31
	s_lshl_b32 s1, s0, 9
	v_writelane_b32 v252, s5, 57
	s_and_b32 s3, s1, 0x200
	s_add_i32 s1, s11, 64
	s_lshl_b64 s[4:5], s[6:7], 10
	v_writelane_b32 v252, s3, 58
	s_add_u32 s3, s38, s3
	s_addc_u32 s13, s39, 0
	s_add_u32 s3, s3, s4
	s_addc_u32 s4, s13, s5
	s_mul_i32 s5, s1, 0xc0000
	s_add_u32 s14, s3, s5
	s_mul_hi_i32 s3, s1, 0xc0000
	s_addc_u32 s15, s4, s3
	s_lshl_b32 s1, s1, 8
	s_ashr_i32 s13, s12, 31
	v_writelane_b32 v252, s1, 59
	s_lshl_b32 s1, s12, 8
	v_writelane_b32 v252, s1, 60
	s_lshl_b64 s[4:5], s[12:13], 18
	v_writelane_b32 v252, s4, 61
	s_mov_b64 s[78:79], 0x40000
	s_mov_b64 s[84:85], 0x80
	v_writelane_b32 v252, s5, 62
	s_lshl_b64 s[4:5], s[6:7], 20
	v_writelane_b32 v252, s4, 63
	s_waitcnt lgkmcnt(0)
	s_barrier
	v_writelane_b32 v253, s5, 0
	s_add_u32 s4, s14, 0x60000
	v_writelane_b32 v253, s14, 1
	s_addc_u32 s5, s15, 0
	s_ashr_i32 s1, s0, 31
	v_writelane_b32 v253, s15, 2
	v_writelane_b32 v253, s4, 3
	s_nop 1
	v_writelane_b32 v253, s5, 4
	s_lshl_b64 s[4:5], s[0:1], 22
	s_lshl_b32 s0, s6, 10
	s_ashr_i32 s1, s0, 31
	s_add_u32 s3, s92, s4
	s_addc_u32 s6, s93, s5
	s_add_u32 s14, s3, 0x5fb61b00
	s_addc_u32 s15, s6, 0
	s_add_u32 s16, s92, 0x61361b00
	s_addc_u32 s17, s93, 0
	s_lshl_b32 s18, s11, 8
	s_mov_b32 s6, s18
	s_ashr_i32 s19, s18, 31
	v_writelane_b32 v253, s6, 5
	s_nop 1
	v_writelane_b32 v253, s7, 6
	s_lshl_b64 s[6:7], s[18:19], 11
	s_add_u32 s18, s14, s6
	v_writelane_b32 v253, s14, 7
	s_addc_u32 s19, s15, s7
	s_lshl_b64 s[42:43], s[12:13], 19
	v_writelane_b32 v253, s15, 8
	s_add_u32 s12, s18, 0x40000
	v_writelane_b32 v253, s18, 9
	s_addc_u32 s13, s19, 0
	s_nop 0
	v_writelane_b32 v253, s19, 10
	v_writelane_b32 v253, s12, 11
	s_nop 1
	v_writelane_b32 v253, s13, 12
	s_add_u32 s12, s16, s4
	v_writelane_b32 v253, s16, 13
	s_addc_u32 s13, s17, s5
	s_cmpk_gt_i32 s28, 0xbf
	v_writelane_b32 v253, s17, 14
	v_writelane_b32 v253, s12, 15
	s_nop 1
	v_writelane_b32 v253, s13, 16
	s_cselect_b64 s[12:13], -1, 0
	v_writelane_b32 v253, s12, 17
	s_add_i32 s3, s89, 0xfffffa00
	s_nop 0
	v_writelane_b32 v253, s13, 18
	v_readlane_b32 s12, v251, 1
	v_readlane_b32 s26, v251, 15
	v_readlane_b32 s13, v251, 2
	v_readlane_b32 s27, v251, 16
	s_add_u32 s12, s26, 0x3000
	v_writelane_b32 v253, s3, 19
	s_addc_u32 s13, s27, 0
	v_readlane_b32 s14, v251, 3
	v_readlane_b32 s15, v251, 4
	v_readlane_b32 s16, v251, 5
	v_readlane_b32 s17, v251, 6
	v_readlane_b32 s18, v251, 7
	v_readlane_b32 s19, v251, 8
	v_readlane_b32 s20, v251, 9
	v_readlane_b32 s21, v251, 10
	v_readlane_b32 s22, v251, 11
	v_readlane_b32 s23, v251, 12
	v_readlane_b32 s24, v251, 13
	v_readlane_b32 s25, v251, 14
	v_writelane_b32 v253, s12, 20
	s_lshl_b32 s3, s28, 6
	s_nop 0
	v_writelane_b32 v253, s13, 21
	v_readlane_b32 s12, v251, 35
	v_readlane_b32 s26, v251, 49
	v_readlane_b32 s13, v251, 36
	v_readlane_b32 s27, v251, 50
	s_add_u32 s12, s26, 0x30000
	v_writelane_b32 v253, s3, 22
	s_addc_u32 s13, s27, 0
	v_writelane_b32 v253, s12, 23
	v_readlane_b32 s14, v251, 37
	v_readlane_b32 s15, v251, 38
	v_writelane_b32 v253, s13, 24
	s_add_u32 s12, s92, 0x37cfdb00
	s_addc_u32 s13, s93, 0
	v_writelane_b32 v253, s12, 25
	s_lshr_b32 s3, s31, 31
	v_readlane_b32 s20, v251, 43
	v_writelane_b32 v253, s13, 26
	v_writelane_b32 v253, s31, 27
	s_add_u32 s12, s28, 0x100
	v_writelane_b32 v253, s3, 28
	s_addc_u32 s13, s29, 0
	s_ashr_i32 s3, s12, 31
	s_lshr_b32 s3, s3, 29
	s_add_i32 s3, s12, s3
	s_ashr_i32 s11, s3, 3
	v_writelane_b32 v253, s11, 29
	s_and_b32 s3, s3, -8
	v_writelane_b32 v253, s12, 30
	s_sub_i32 s3, s12, s3
	s_mov_b32 s20, 0
	v_writelane_b32 v253, s13, 31
	v_writelane_b32 v253, s3, 32
	s_lshr_b32 s3, s3, 31
	s_add_u32 s12, s28, 0x200
	v_writelane_b32 v253, s3, 33
	s_addc_u32 s13, s29, 0
	s_ashr_i32 s3, s12, 31
	s_lshr_b32 s3, s3, 29
	s_add_i32 s3, s12, s3
	s_ashr_i32 s11, s3, 3
	v_writelane_b32 v253, s11, 34
	s_and_b32 s3, s3, -8
	v_writelane_b32 v253, s12, 35
	s_sub_i32 s3, s12, s3
	v_readlane_b32 s16, v251, 39
	v_writelane_b32 v253, s13, 36
	v_writelane_b32 v253, s3, 37
	s_lshr_b32 s3, s3, 31
	s_add_u32 s12, s28, 0x300
	v_writelane_b32 v253, s3, 38
	s_addc_u32 s13, s29, 0
	s_ashr_i32 s3, s12, 31
	s_lshr_b32 s3, s3, 29
	s_add_i32 s3, s12, s3
	s_ashr_i32 s11, s3, 3
	v_writelane_b32 v253, s11, 39
	s_and_b32 s3, s3, -8
	v_writelane_b32 v253, s12, 40
	s_sub_i32 s3, s12, s3
	v_readlane_b32 s17, v251, 40
	v_writelane_b32 v253, s13, 41
	v_writelane_b32 v253, s3, 42
	s_lshr_b32 s3, s3, 31
	s_add_u32 s12, s28, 0x400
	v_writelane_b32 v253, s3, 43
	s_addc_u32 s13, s29, 0
	s_ashr_i32 s3, s12, 31
	s_lshr_b32 s3, s3, 29
	s_add_i32 s3, s12, s3
	s_ashr_i32 s11, s3, 3
	v_writelane_b32 v253, s11, 44
	s_and_b32 s3, s3, -8
	v_writelane_b32 v253, s12, 45
	s_sub_i32 s3, s12, s3
	v_readlane_b32 s18, v251, 41
	v_writelane_b32 v253, s13, 46
	v_writelane_b32 v253, s3, 47
	s_lshr_b32 s3, s3, 31
	s_add_u32 s12, s28, 0x500
	v_writelane_b32 v253, s3, 48
	s_addc_u32 s13, s29, 0
	s_ashr_i32 s3, s12, 31
	s_lshr_b32 s3, s3, 29
	s_add_i32 s3, s12, s3
	s_ashr_i32 s11, s3, 3
	v_writelane_b32 v253, s11, 49
	s_and_b32 s3, s3, -8
	v_writelane_b32 v253, s12, 50
	s_sub_i32 s3, s12, s3
	v_readlane_b32 s19, v251, 42
	v_writelane_b32 v253, s13, 51
	v_writelane_b32 v253, s3, 52
	s_lshr_b32 s3, s3, 31
	s_add_u32 s12, s28, 0x600
	v_writelane_b32 v253, s3, 53
	s_addc_u32 s13, s29, 0
	s_ashr_i32 s3, s12, 31
	s_lshr_b32 s3, s3, 29
	s_add_i32 s3, s12, s3
	s_ashr_i32 s11, s3, 3
	v_writelane_b32 v253, s11, 54
	s_and_b32 s3, s3, -8
	v_writelane_b32 v253, s12, 55
	s_sub_i32 s3, s12, s3
	v_readlane_b32 s21, v251, 44
	v_writelane_b32 v253, s13, 56
	v_writelane_b32 v253, s3, 57
	s_lshr_b32 s3, s3, 31
	s_add_u32 s12, s28, 0x700
	v_writelane_b32 v253, s3, 58
	s_addc_u32 s13, s29, 0
	s_ashr_i32 s3, s12, 31
	s_lshr_b32 s3, s3, 29
	s_add_i32 s3, s12, s3
	s_ashr_i32 s11, s3, 3
	v_writelane_b32 v253, s11, 59
	s_and_b32 s3, s3, -8
	v_writelane_b32 v253, s12, 60
	s_sub_i32 s3, s12, s3
	v_readlane_b32 s22, v251, 45
	v_writelane_b32 v253, s13, 61
	v_writelane_b32 v253, s3, 62
	s_lshr_b32 s3, s3, 31
	s_add_u32 s12, s28, 0x800
	v_writelane_b32 v253, s3, 63
	s_addc_u32 s13, s29, 0
	s_ashr_i32 s3, s12, 31
	s_lshr_b32 s3, s3, 29
	s_add_i32 s3, s12, s3
	s_ashr_i32 s11, s3, 3
	v_writelane_b32 v254, s11, 1
	s_and_b32 s3, s3, -8
	v_writelane_b32 v254, s12, 2
	s_sub_i32 s3, s12, s3
	v_readlane_b32 s23, v251, 46
	v_writelane_b32 v254, s13, 3
	v_writelane_b32 v254, s3, 4
	s_lshr_b32 s3, s3, 31
	s_add_u32 s12, s92, 0x37d21b00
	v_writelane_b32 v254, s3, 5
	s_addc_u32 s13, s93, 0
	v_writelane_b32 v254, s12, 6
	v_readlane_b32 s24, v251, 47
	v_readlane_b32 s25, v251, 48
	v_writelane_b32 v254, s13, 7
	s_add_u32 s12, s92, 0x48db680
	s_addc_u32 s13, s93, 0
	v_writelane_b32 v254, s12, 8
	s_cmp_lt_i32 s28, 64
	s_nop 0
	v_writelane_b32 v254, s13, 9
	s_cselect_b64 s[12:13], -1, 0
	v_writelane_b32 v254, s12, 10
	s_add_i32 s3, s89, 0xfffffe00
	s_nop 0
	v_writelane_b32 v254, s13, 11
	v_writelane_b32 v254, s3, 12
	s_add_u32 s12, s34, 0x40000
	v_writelane_b32 v254, s34, 13
	s_addc_u32 s13, s35, 0
	s_cmpk_lt_u32 s28, 0xa0
	v_writelane_b32 v254, s35, 14
	v_writelane_b32 v254, s12, 15
	s_cselect_b32 s3, s10, s9
	s_cselect_b32 s9, 6, 0x72
	s_cmpk_lt_i32 s28, 0x80
	s_mul_i32 s10, s28, 57
	v_writelane_b32 v254, s13, 16
	s_cselect_b32 s11, s10, s3
	s_cselect_b32 s12, 57, s9
	s_add_i32 s3, s8, s30
	s_ashr_i32 s8, s3, 31
	s_lshr_b32 s8, s8, 27
	s_add_i32 s8, s3, s8
	s_and_b32 s9, s8, 0xffe0
	s_sub_i32 s3, s3, s9
	s_bfe_i32 s9, s3, 0x80000
	s_bfe_u32 s9, s9, 0x3000c
	s_add_i32 s9, s3, s9
	s_and_b32 s10, s9, 0xf8
	v_writelane_b32 v254, s30, 17
	s_sub_i32 s3, s3, s10
	s_ashr_i32 s8, s8, 5
	s_lshl_b32 s8, s8, 3
	s_bfe_i32 s9, s9, 0x80000
	s_sext_i32_i8 s3, s3
	v_writelane_b32 v254, s11, 18
	s_sext_i32_i16 s9, s9
	s_add_i32 s14, s8, s3
	v_writelane_b32 v254, s12, 19
	s_add_i32 s3, s11, s12
	v_writelane_b32 v254, s3, 20
	s_ashr_i32 s3, s9, 3
	s_ashr_i32 s15, s14, 31
	v_writelane_b32 v254, s3, 21
	s_lshr_b32 s8, s9, 3
	s_mul_i32 s9, s14, 0xc0000
	s_mul_hi_i32 s3, s14, 0xc0000
	s_add_u32 s10, s38, s9
	v_writelane_b32 v254, s38, 22
	s_addc_u32 s11, s39, s3
	s_bfe_i64 s[8:9], s[8:9], 0x100000
	v_writelane_b32 v254, s39, 23
	v_writelane_b32 v254, s10, 24
	s_nop 1
	v_writelane_b32 v254, s11, 25
	s_lshl_b64 s[10:11], s[8:9], 18
	v_writelane_b32 v254, s10, 26
	s_nop 1
	v_writelane_b32 v254, s11, 27
	s_mov_b32 s10, s14
	v_writelane_b32 v254, s10, 28
	s_nop 1
	v_writelane_b32 v254, s11, 29
	s_lshl_b64 s[10:11], s[14:15], 19
	s_add_u32 s10, s40, s10
	v_writelane_b32 v254, s40, 30
	s_addc_u32 s11, s41, s11
	s_lshl_b64 s[8:9], s[8:9], 19
	v_writelane_b32 v254, s41, 31
	v_writelane_b32 v254, s8, 32
	s_nop 1
	v_writelane_b32 v254, s9, 33
	s_add_u32 s8, s10, 0x40000
	v_writelane_b32 v254, s10, 34
	s_addc_u32 s9, s11, 0
	s_add_i32 s3, s33, 0xfffe0000
	v_writelane_b32 v254, s11, 35
	v_writelane_b32 v254, s8, 36
	s_nop 1
	v_writelane_b32 v254, s9, 37
	v_writelane_b32 v254, s33, 38
	v_writelane_b32 v254, s3, 39
	s_lshl_b64 s[8:9], s[36:37], 1
	v_writelane_b32 v254, s8, 40
	s_add_u32 s3, s92, 0x462a9b00
	s_movk_i32 s33, 0x1b10
	v_writelane_b32 v254, s9, 41
	v_writelane_b32 v254, s3, 42
	s_addc_u32 s3, s93, 0
	s_add_u32 s8, s92, 0x276ddd00
	v_writelane_b32 v254, s3, 43
	s_addc_u32 s9, s93, 0
	v_writelane_b32 v254, s8, 44
	s_add_u32 s3, s4, s6
	s_addc_u32 s4, s5, s7
	v_writelane_b32 v254, s9, 45
	s_mul_hi_i32 s5, s2, 56
	v_writelane_b32 v254, s5, 46
	s_mul_i32 s2, s2, 56
	v_writelane_b32 v254, s2, 47
	s_mul_hi_i32 s7, s36, 10
	v_writelane_b32 v254, s36, 48
	s_mul_i32 s6, s36, 10
	s_add_u32 s2, s92, s3
	v_writelane_b32 v254, s37, 49
	v_writelane_b32 v254, s6, 50
	s_addc_u32 s3, s93, s4
	s_nop 0
	v_writelane_b32 v254, s7, 51
	v_writelane_b32 v254, s2, 52
	s_add_u32 s2, s2, 0x5fba1b80
	v_writelane_b32 v254, s3, 53
	s_addc_u32 s3, s3, 0
	v_writelane_b32 v254, s2, 54
	s_nop 1
	v_writelane_b32 v254, s3, 55
	s_add_u32 s2, s92, s42
	v_writelane_b32 v254, s42, 56
	s_addc_u32 s3, s93, s43
	s_add_u32 s2, s2, 0x46621c00
	v_writelane_b32 v254, s43, 57
	v_writelane_b32 v254, s2, 58
	s_addc_u32 s2, s3, 0
	v_writelane_b32 v254, s2, 59
	s_lshl_b64 s[0:1], s[0:1], 1
	v_writelane_b32 v254, s0, 60
	s_nop 1
	v_writelane_b32 v254, s1, 61
	s_add_i32 s0, 0, 0x27f00
	v_writelane_b32 v254, s0, 62
	s_add_i32 s0, 0, 0x27f04
	v_writelane_b32 v254, s0, 63
	s_add_i32 s0, 0, 0x27700
	v_writelane_b32 v255, s0, 0
	s_add_i32 s0, 0, 0x4400
	v_writelane_b32 v255, s0, 1
	s_add_i32 s0, 0, 0x10800
	v_writelane_b32 v255, s0, 2
	s_add_i32 s0, 0, 0x14800
	v_writelane_b32 v255, s0, 3
	s_add_i32 s0, 0, 0x18c00
	v_writelane_b32 v255, s0, 4
	s_add_i32 s0, 0, 0x20200
	v_writelane_b32 v255, s0, 5
	s_mov_b32 s1, 0
	v_writelane_b32 v255, s0, 6
	s_nop 1
	v_writelane_b32 v255, s1, 7
	v_writelane_b32 v255, s64, 8
	s_nop 1
	v_writelane_b32 v255, s65, 9
	v_writelane_b32 v255, s66, 10
	v_writelane_b32 v255, s67, 11
	v_writelane_b32 v255, s68, 12
	v_writelane_b32 v255, s69, 13
	v_writelane_b32 v255, s70, 14
	v_writelane_b32 v255, s71, 15
	v_writelane_b32 v255, s74, 16
	v_writelane_b32 v255, s72, 17
	s_nop 1
	v_writelane_b32 v255, s73, 18
	v_writelane_b32 v255, s86, 19
	s_nop 1
	v_writelane_b32 v255, s87, 20
	v_writelane_b32 v255, s94, 21
	s_nop 1
	v_writelane_b32 v255, s95, 22
	v_writelane_b32 v255, s96, 23
	s_nop 1
	v_writelane_b32 v255, s97, 24
	v_writelane_b32 v255, s60, 25
	s_nop 1
	v_writelane_b32 v255, s61, 26
	v_writelane_b32 v255, s89, 27
	s_branch .LBB0_67

.LBB0_216:
	v_lshl_or_b32 v142, s27, 8, v148
	s_cmp_gt_i32 s27, 14
	s_movk_i32 s7, 0xf0f
	s_cselect_b64 s[14:15], -1, 0
	v_cmp_lt_i32_e32 vcc, s7, v142
	s_and_b64 s[12:13], s[14:15], vcc
	s_and_saveexec_b64 s[16:17], s[12:13]
	s_cbranch_execz .LBB0_218
	s_mov_b32 s7, 0xc1f00000
	v_med3_f32 v126, v126, s7, v233
	v_med3_f32 v122, v122, s7, v233
	v_med3_f32 v127, v127, s7, v233
	v_med3_f32 v123, v123, s7, v233
	v_med3_f32 v128, v128, s7, v233
	v_med3_f32 v124, v124, s7, v233
	v_med3_f32 v129, v129, s7, v233
	v_med3_f32 v125, v125, s7, v233
	v_mul_f32_e32 v126, 0xbfb8aa3b, v126
	v_mul_f32_e32 v122, 0xbfb8aa3b, v122
	v_mul_f32_e32 v127, 0xbfb8aa3b, v127
	v_mul_f32_e32 v123, 0xbfb8aa3b, v123
	v_mul_f32_e32 v128, 0xbfb8aa3b, v128
	v_mul_f32_e32 v124, 0xbfb8aa3b, v124
	v_mul_f32_e32 v129, 0xbfb8aa3b, v129
	v_mul_f32_e32 v125, 0xbfb8aa3b, v125
	v_exp_f32_e32 v126, v126
	v_exp_f32_e32 v122, v122
	v_exp_f32_e32 v127, v127
	v_exp_f32_e32 v123, v123
	v_exp_f32_e32 v128, v128
	v_exp_f32_e32 v124, v124
	v_exp_f32_e32 v129, v129
	v_exp_f32_e32 v125, v125
	v_add_f32_e32 v126, 1.0, v126
	v_add_f32_e32 v122, 1.0, v122
	v_add_f32_e32 v127, 1.0, v127
	v_add_f32_e32 v123, 1.0, v123
	v_add_f32_e32 v128, 1.0, v128
	v_add_f32_e32 v124, 1.0, v124
	v_add_f32_e32 v129, 1.0, v129
	v_add_f32_e32 v125, 1.0, v125
	v_rcp_f32_e32 v126, v126
	v_rcp_f32_e32 v122, v122
	v_rcp_f32_e32 v127, v127
	v_rcp_f32_e32 v123, v123
	v_rcp_f32_e32 v128, v128
	v_rcp_f32_e32 v124, v124
	v_rcp_f32_e32 v129, v129
	v_rcp_f32_e32 v125, v125
.LBB0_218:
	s_or_b64 exec, exec, s[16:17]
	v_readlane_b32 s16, v252, 3
	v_readlane_b32 s17, v252, 4
	v_lshl_add_u32 v150, s26, 8, v146
	v_cvt_pk_bf16_f32 v126, v126, v127
	v_cvt_pk_bf16_f32 v127, v128, v129
	v_cvt_pk_bf16_f32 v128, v122, v123
	v_or_b32_e32 v122, 0x80, v142
	v_mov_b64_e32 v[144:145], s[16:17]
	s_movk_i32 s7, 0xf0f
	v_ashrrev_i32_e32 v143, 31, v142
	v_mad_i64_i32 v[144:145], s[16:17], v150, s81, v[144:145]
	v_cmp_lt_i32_e32 vcc, s7, v122
	v_lshl_add_u64 v[144:145], v[142:143], 1, v[144:145]
	s_and_b64 s[14:15], s[14:15], vcc
	v_cvt_pk_bf16_f32 v129, v124, v125
	global_store_dwordx4 v[144:145], v[126:129], off
	s_and_saveexec_b64 s[16:17], s[14:15]
	s_cbranch_execz .LBB0_220
	s_mov_b32 s7, 0xc1f00000
	v_med3_f32 v118, v118, s7, v233
	v_med3_f32 v114, v114, s7, v233
	v_med3_f32 v119, v119, s7, v233
	v_med3_f32 v115, v115, s7, v233
	v_med3_f32 v120, v120, s7, v233
	v_med3_f32 v116, v116, s7, v233
	v_med3_f32 v121, v121, s7, v233
	v_med3_f32 v117, v117, s7, v233
	v_mul_f32_e32 v118, 0xbfb8aa3b, v118
	v_mul_f32_e32 v114, 0xbfb8aa3b, v114
	v_mul_f32_e32 v119, 0xbfb8aa3b, v119
	v_mul_f32_e32 v115, 0xbfb8aa3b, v115
	v_mul_f32_e32 v120, 0xbfb8aa3b, v120
	v_mul_f32_e32 v116, 0xbfb8aa3b, v116
	v_mul_f32_e32 v121, 0xbfb8aa3b, v121
	v_mul_f32_e32 v117, 0xbfb8aa3b, v117
	v_exp_f32_e32 v118, v118
	v_exp_f32_e32 v114, v114
	v_exp_f32_e32 v119, v119
	v_exp_f32_e32 v115, v115
	v_exp_f32_e32 v120, v120
	v_exp_f32_e32 v116, v116
	v_exp_f32_e32 v121, v121
	v_exp_f32_e32 v117, v117
	v_add_f32_e32 v118, 1.0, v118
	v_add_f32_e32 v114, 1.0, v114
	v_add_f32_e32 v119, 1.0, v119
	v_add_f32_e32 v115, 1.0, v115
	v_add_f32_e32 v120, 1.0, v120
	v_add_f32_e32 v116, 1.0, v116
	v_add_f32_e32 v121, 1.0, v121
	v_add_f32_e32 v117, 1.0, v117
	v_rcp_f32_e32 v118, v118
	v_rcp_f32_e32 v114, v114
	v_rcp_f32_e32 v119, v119
	v_rcp_f32_e32 v115, v115
	v_rcp_f32_e32 v120, v120
	v_rcp_f32_e32 v116, v116
	v_rcp_f32_e32 v121, v121
	v_rcp_f32_e32 v117, v117
.LBB0_220:
	s_or_b64 exec, exec, s[16:17]
	v_cvt_pk_bf16_f32 v118, v118, v119
	v_cvt_pk_bf16_f32 v119, v120, v121
	v_cvt_pk_bf16_f32 v120, v114, v115
	v_cvt_pk_bf16_f32 v121, v116, v117
	global_store_dwordx4 v[144:145], v[118:121], off offset:256
	s_and_saveexec_b64 s[16:17], s[12:13]
	s_cbranch_execz .LBB0_222
	s_mov_b32 s7, 0xc1f00000
	v_med3_f32 v110, v110, s7, v233
	v_med3_f32 v106, v106, s7, v233
	v_med3_f32 v111, v111, s7, v233
	v_med3_f32 v107, v107, s7, v233
	v_med3_f32 v112, v112, s7, v233
	v_med3_f32 v108, v108, s7, v233
	v_med3_f32 v113, v113, s7, v233
	v_med3_f32 v109, v109, s7, v233
	v_mul_f32_e32 v110, 0xbfb8aa3b, v110
	v_mul_f32_e32 v106, 0xbfb8aa3b, v106
	v_mul_f32_e32 v111, 0xbfb8aa3b, v111
	v_mul_f32_e32 v107, 0xbfb8aa3b, v107
	v_mul_f32_e32 v112, 0xbfb8aa3b, v112
	v_mul_f32_e32 v108, 0xbfb8aa3b, v108
	v_mul_f32_e32 v113, 0xbfb8aa3b, v113
	v_mul_f32_e32 v109, 0xbfb8aa3b, v109
	v_exp_f32_e32 v110, v110
	v_exp_f32_e32 v106, v106
	v_exp_f32_e32 v111, v111
	v_exp_f32_e32 v107, v107
	v_exp_f32_e32 v112, v112
	v_exp_f32_e32 v108, v108
	v_exp_f32_e32 v113, v113
	v_exp_f32_e32 v109, v109
	v_add_f32_e32 v110, 1.0, v110
	v_add_f32_e32 v106, 1.0, v106
	v_add_f32_e32 v111, 1.0, v111
	v_add_f32_e32 v107, 1.0, v107
	v_add_f32_e32 v112, 1.0, v112
	v_add_f32_e32 v108, 1.0, v108
	v_add_f32_e32 v113, 1.0, v113
	v_add_f32_e32 v109, 1.0, v109
	v_rcp_f32_e32 v110, v110
	v_rcp_f32_e32 v106, v106
	v_rcp_f32_e32 v111, v111
	v_rcp_f32_e32 v107, v107
	v_rcp_f32_e32 v112, v112
	v_rcp_f32_e32 v108, v108
	v_rcp_f32_e32 v113, v113
	v_rcp_f32_e32 v109, v109
.LBB0_222:
	s_or_b64 exec, exec, s[16:17]
	v_readlane_b32 s16, v252, 3
	v_readlane_b32 s17, v252, 4
	v_or_b32_e32 v116, 16, v150
	v_cvt_pk_bf16_f32 v110, v110, v111
	v_cvt_pk_bf16_f32 v111, v112, v113
	v_cvt_pk_bf16_f32 v112, v106, v107
	v_cvt_pk_bf16_f32 v113, v108, v109
	s_nop 0
	v_mov_b64_e32 v[114:115], s[16:17]
	v_mad_i64_i32 v[114:115], s[16:17], v116, s81, v[114:115]
	v_lshl_add_u64 v[114:115], v[142:143], 1, v[114:115]
	global_store_dwordx4 v[114:115], v[110:113], off
	s_and_saveexec_b64 s[16:17], s[14:15]
	s_cbranch_execz .LBB0_224
	s_mov_b32 s7, 0xc1f00000
	v_med3_f32 v102, v102, s7, v233
	v_med3_f32 v98, v98, s7, v233
	v_med3_f32 v103, v103, s7, v233
	v_med3_f32 v99, v99, s7, v233
	v_med3_f32 v104, v104, s7, v233
	v_med3_f32 v100, v100, s7, v233
	v_med3_f32 v105, v105, s7, v233
	v_med3_f32 v101, v101, s7, v233
	v_mul_f32_e32 v102, 0xbfb8aa3b, v102
	v_mul_f32_e32 v98, 0xbfb8aa3b, v98
	v_mul_f32_e32 v103, 0xbfb8aa3b, v103
	v_mul_f32_e32 v99, 0xbfb8aa3b, v99
	v_mul_f32_e32 v104, 0xbfb8aa3b, v104
	v_mul_f32_e32 v100, 0xbfb8aa3b, v100
	v_mul_f32_e32 v105, 0xbfb8aa3b, v105
	v_mul_f32_e32 v101, 0xbfb8aa3b, v101
	v_exp_f32_e32 v102, v102
	v_exp_f32_e32 v98, v98
	v_exp_f32_e32 v103, v103
	v_exp_f32_e32 v99, v99
	v_exp_f32_e32 v104, v104
	v_exp_f32_e32 v100, v100
	v_exp_f32_e32 v105, v105
	v_exp_f32_e32 v101, v101
	v_add_f32_e32 v102, 1.0, v102
	v_add_f32_e32 v98, 1.0, v98
	v_add_f32_e32 v103, 1.0, v103
	v_add_f32_e32 v99, 1.0, v99
	v_add_f32_e32 v104, 1.0, v104
	v_add_f32_e32 v100, 1.0, v100
	v_add_f32_e32 v105, 1.0, v105
	v_add_f32_e32 v101, 1.0, v101
	v_rcp_f32_e32 v102, v102
	v_rcp_f32_e32 v98, v98
	v_rcp_f32_e32 v103, v103
	v_rcp_f32_e32 v99, v99
	v_rcp_f32_e32 v104, v104
	v_rcp_f32_e32 v100, v100
	v_rcp_f32_e32 v105, v105
	v_rcp_f32_e32 v101, v101
.LBB0_224:
	s_or_b64 exec, exec, s[16:17]
	v_cvt_pk_bf16_f32 v102, v102, v103
	v_cvt_pk_bf16_f32 v103, v104, v105
	v_cvt_pk_bf16_f32 v104, v98, v99
	v_cvt_pk_bf16_f32 v105, v100, v101
	global_store_dwordx4 v[114:115], v[102:105], off offset:256
	s_and_saveexec_b64 s[16:17], s[12:13]
	s_cbranch_execz .LBB0_226
	s_mov_b32 s7, 0xc1f00000
	v_med3_f32 v94, v94, s7, v233
	v_med3_f32 v90, v90, s7, v233
	v_med3_f32 v95, v95, s7, v233
	v_med3_f32 v91, v91, s7, v233
	v_med3_f32 v96, v96, s7, v233
	v_med3_f32 v92, v92, s7, v233
	v_med3_f32 v97, v97, s7, v233
	v_med3_f32 v93, v93, s7, v233
	v_mul_f32_e32 v94, 0xbfb8aa3b, v94
	v_mul_f32_e32 v90, 0xbfb8aa3b, v90
	v_mul_f32_e32 v95, 0xbfb8aa3b, v95
	v_mul_f32_e32 v91, 0xbfb8aa3b, v91
	v_mul_f32_e32 v96, 0xbfb8aa3b, v96
	v_mul_f32_e32 v92, 0xbfb8aa3b, v92
	v_mul_f32_e32 v97, 0xbfb8aa3b, v97
	v_mul_f32_e32 v93, 0xbfb8aa3b, v93
	v_exp_f32_e32 v94, v94
	v_exp_f32_e32 v90, v90
	v_exp_f32_e32 v95, v95
	v_exp_f32_e32 v91, v91
	v_exp_f32_e32 v96, v96
	v_exp_f32_e32 v92, v92
	v_exp_f32_e32 v97, v97
	v_exp_f32_e32 v93, v93
	v_add_f32_e32 v94, 1.0, v94
	v_add_f32_e32 v90, 1.0, v90
	v_add_f32_e32 v95, 1.0, v95
	v_add_f32_e32 v91, 1.0, v91
	v_add_f32_e32 v96, 1.0, v96
	v_add_f32_e32 v92, 1.0, v92
	v_add_f32_e32 v97, 1.0, v97
	v_add_f32_e32 v93, 1.0, v93
	v_rcp_f32_e32 v94, v94
	v_rcp_f32_e32 v90, v90
	v_rcp_f32_e32 v95, v95
	v_rcp_f32_e32 v91, v91
	v_rcp_f32_e32 v96, v96
	v_rcp_f32_e32 v92, v92
	v_rcp_f32_e32 v97, v97
	v_rcp_f32_e32 v93, v93
.LBB0_226:
	s_or_b64 exec, exec, s[16:17]
	v_readlane_b32 s16, v252, 3
	v_readlane_b32 s17, v252, 4
	v_or_b32_e32 v100, 32, v150
	v_cvt_pk_bf16_f32 v94, v94, v95
	v_cvt_pk_bf16_f32 v95, v96, v97
	v_cvt_pk_bf16_f32 v96, v90, v91
	v_cvt_pk_bf16_f32 v97, v92, v93
	s_nop 0
	v_mov_b64_e32 v[98:99], s[16:17]
	v_mad_i64_i32 v[98:99], s[16:17], v100, s81, v[98:99]
	v_lshl_add_u64 v[98:99], v[142:143], 1, v[98:99]
	global_store_dwordx4 v[98:99], v[94:97], off
	s_and_saveexec_b64 s[16:17], s[14:15]
	s_cbranch_execz .LBB0_228
	s_mov_b32 s7, 0xc1f00000
	v_med3_f32 v86, v86, s7, v233
	v_med3_f32 v82, v82, s7, v233
	v_med3_f32 v87, v87, s7, v233
	v_med3_f32 v83, v83, s7, v233
	v_med3_f32 v88, v88, s7, v233
	v_med3_f32 v84, v84, s7, v233
	v_med3_f32 v89, v89, s7, v233
	v_med3_f32 v85, v85, s7, v233
	v_mul_f32_e32 v86, 0xbfb8aa3b, v86
	v_mul_f32_e32 v82, 0xbfb8aa3b, v82
	v_mul_f32_e32 v87, 0xbfb8aa3b, v87
	v_mul_f32_e32 v83, 0xbfb8aa3b, v83
	v_mul_f32_e32 v88, 0xbfb8aa3b, v88
	v_mul_f32_e32 v84, 0xbfb8aa3b, v84
	v_mul_f32_e32 v89, 0xbfb8aa3b, v89
	v_mul_f32_e32 v85, 0xbfb8aa3b, v85
	v_exp_f32_e32 v86, v86
	v_exp_f32_e32 v82, v82
	v_exp_f32_e32 v87, v87
	v_exp_f32_e32 v83, v83
	v_exp_f32_e32 v88, v88
	v_exp_f32_e32 v84, v84
	v_exp_f32_e32 v89, v89
	v_exp_f32_e32 v85, v85
	v_add_f32_e32 v86, 1.0, v86
	v_add_f32_e32 v82, 1.0, v82
	v_add_f32_e32 v87, 1.0, v87
	v_add_f32_e32 v83, 1.0, v83
	v_add_f32_e32 v88, 1.0, v88
	v_add_f32_e32 v84, 1.0, v84
	v_add_f32_e32 v89, 1.0, v89
	v_add_f32_e32 v85, 1.0, v85
	v_rcp_f32_e32 v86, v86
	v_rcp_f32_e32 v82, v82
	v_rcp_f32_e32 v87, v87
	v_rcp_f32_e32 v83, v83
	v_rcp_f32_e32 v88, v88
	v_rcp_f32_e32 v84, v84
	v_rcp_f32_e32 v89, v89
	v_rcp_f32_e32 v85, v85
.LBB0_228:
	s_or_b64 exec, exec, s[16:17]
	v_cvt_pk_bf16_f32 v86, v86, v87
	v_cvt_pk_bf16_f32 v87, v88, v89
	v_cvt_pk_bf16_f32 v88, v82, v83
	v_cvt_pk_bf16_f32 v89, v84, v85
	global_store_dwordx4 v[98:99], v[86:89], off offset:256
	s_and_saveexec_b64 s[16:17], s[12:13]
	s_cbranch_execz .LBB0_230
	s_mov_b32 s7, 0xc1f00000
	v_med3_f32 v78, v78, s7, v233
	v_med3_f32 v74, v74, s7, v233
	v_med3_f32 v79, v79, s7, v233
	v_med3_f32 v75, v75, s7, v233
	v_med3_f32 v80, v80, s7, v233
	v_med3_f32 v76, v76, s7, v233
	v_med3_f32 v81, v81, s7, v233
	v_med3_f32 v77, v77, s7, v233
	v_mul_f32_e32 v78, 0xbfb8aa3b, v78
	v_mul_f32_e32 v74, 0xbfb8aa3b, v74
	v_mul_f32_e32 v79, 0xbfb8aa3b, v79
	v_mul_f32_e32 v75, 0xbfb8aa3b, v75
	v_mul_f32_e32 v80, 0xbfb8aa3b, v80
	v_mul_f32_e32 v76, 0xbfb8aa3b, v76
	v_mul_f32_e32 v81, 0xbfb8aa3b, v81
	v_mul_f32_e32 v77, 0xbfb8aa3b, v77
	v_exp_f32_e32 v78, v78
	v_exp_f32_e32 v74, v74
	v_exp_f32_e32 v79, v79
	v_exp_f32_e32 v75, v75
	v_exp_f32_e32 v80, v80
	v_exp_f32_e32 v76, v76
	v_exp_f32_e32 v81, v81
	v_exp_f32_e32 v77, v77
	v_add_f32_e32 v78, 1.0, v78
	v_add_f32_e32 v74, 1.0, v74
	v_add_f32_e32 v79, 1.0, v79
	v_add_f32_e32 v75, 1.0, v75
	v_add_f32_e32 v80, 1.0, v80
	v_add_f32_e32 v76, 1.0, v76
	v_add_f32_e32 v81, 1.0, v81
	v_add_f32_e32 v77, 1.0, v77
	v_rcp_f32_e32 v78, v78
	v_rcp_f32_e32 v74, v74
	v_rcp_f32_e32 v79, v79
	v_rcp_f32_e32 v75, v75
	v_rcp_f32_e32 v80, v80
	v_rcp_f32_e32 v76, v76
	v_rcp_f32_e32 v81, v81
	v_rcp_f32_e32 v77, v77
.LBB0_230:
	s_or_b64 exec, exec, s[16:17]
	v_readlane_b32 s16, v252, 3
	v_readlane_b32 s17, v252, 4
	v_or_b32_e32 v84, 48, v150
	v_cvt_pk_bf16_f32 v78, v78, v79
	v_cvt_pk_bf16_f32 v79, v80, v81
	v_cvt_pk_bf16_f32 v80, v74, v75
	v_cvt_pk_bf16_f32 v81, v76, v77
	s_nop 0
	v_mov_b64_e32 v[82:83], s[16:17]
	v_mad_i64_i32 v[82:83], s[16:17], v84, s81, v[82:83]
	v_lshl_add_u64 v[82:83], v[142:143], 1, v[82:83]
	global_store_dwordx4 v[82:83], v[78:81], off
	s_and_saveexec_b64 s[16:17], s[14:15]
	s_cbranch_execz .LBB0_232
	s_mov_b32 s7, 0xc1f00000
	v_med3_f32 v70, v70, s7, v233
	v_med3_f32 v66, v66, s7, v233
	v_med3_f32 v71, v71, s7, v233
	v_med3_f32 v67, v67, s7, v233
	v_med3_f32 v72, v72, s7, v233
	v_med3_f32 v68, v68, s7, v233
	v_med3_f32 v73, v73, s7, v233
	v_med3_f32 v69, v69, s7, v233
	v_mul_f32_e32 v70, 0xbfb8aa3b, v70
	v_mul_f32_e32 v66, 0xbfb8aa3b, v66
	v_mul_f32_e32 v71, 0xbfb8aa3b, v71
	v_mul_f32_e32 v67, 0xbfb8aa3b, v67
	v_mul_f32_e32 v72, 0xbfb8aa3b, v72
	v_mul_f32_e32 v68, 0xbfb8aa3b, v68
	v_mul_f32_e32 v73, 0xbfb8aa3b, v73
	v_mul_f32_e32 v69, 0xbfb8aa3b, v69
	v_exp_f32_e32 v70, v70
	v_exp_f32_e32 v66, v66
	v_exp_f32_e32 v71, v71
	v_exp_f32_e32 v67, v67
	v_exp_f32_e32 v72, v72
	v_exp_f32_e32 v68, v68
	v_exp_f32_e32 v73, v73
	v_exp_f32_e32 v69, v69
	v_add_f32_e32 v70, 1.0, v70
	v_add_f32_e32 v66, 1.0, v66
	v_add_f32_e32 v71, 1.0, v71
	v_add_f32_e32 v67, 1.0, v67
	v_add_f32_e32 v72, 1.0, v72
	v_add_f32_e32 v68, 1.0, v68
	v_add_f32_e32 v73, 1.0, v73
	v_add_f32_e32 v69, 1.0, v69
	v_rcp_f32_e32 v70, v70
	v_rcp_f32_e32 v66, v66
	v_rcp_f32_e32 v71, v71
	v_rcp_f32_e32 v67, v67
	v_rcp_f32_e32 v72, v72
	v_rcp_f32_e32 v68, v68
	v_rcp_f32_e32 v73, v73
	v_rcp_f32_e32 v69, v69
.LBB0_232:
	s_or_b64 exec, exec, s[16:17]
	v_cvt_pk_bf16_f32 v70, v70, v71
	v_cvt_pk_bf16_f32 v71, v72, v73
	v_cvt_pk_bf16_f32 v72, v66, v67
	v_cvt_pk_bf16_f32 v73, v68, v69
	global_store_dwordx4 v[82:83], v[70:73], off offset:256
	s_and_saveexec_b64 s[16:17], s[12:13]
	s_cbranch_execz .LBB0_234
	s_mov_b32 s7, 0xc1f00000
	v_med3_f32 v62, v62, s7, v233
	v_med3_f32 v58, v58, s7, v233
	v_med3_f32 v63, v63, s7, v233
	v_med3_f32 v59, v59, s7, v233
	v_med3_f32 v64, v64, s7, v233
	v_med3_f32 v60, v60, s7, v233
	v_med3_f32 v65, v65, s7, v233
	v_med3_f32 v61, v61, s7, v233
	v_mul_f32_e32 v62, 0xbfb8aa3b, v62
	v_mul_f32_e32 v58, 0xbfb8aa3b, v58
	v_mul_f32_e32 v63, 0xbfb8aa3b, v63
	v_mul_f32_e32 v59, 0xbfb8aa3b, v59
	v_mul_f32_e32 v64, 0xbfb8aa3b, v64
	v_mul_f32_e32 v60, 0xbfb8aa3b, v60
	v_mul_f32_e32 v65, 0xbfb8aa3b, v65
	v_mul_f32_e32 v61, 0xbfb8aa3b, v61
	v_exp_f32_e32 v62, v62
	v_exp_f32_e32 v58, v58
	v_exp_f32_e32 v63, v63
	v_exp_f32_e32 v59, v59
	v_exp_f32_e32 v64, v64
	v_exp_f32_e32 v60, v60
	v_exp_f32_e32 v65, v65
	v_exp_f32_e32 v61, v61
	v_add_f32_e32 v62, 1.0, v62
	v_add_f32_e32 v58, 1.0, v58
	v_add_f32_e32 v63, 1.0, v63
	v_add_f32_e32 v59, 1.0, v59
	v_add_f32_e32 v64, 1.0, v64
	v_add_f32_e32 v60, 1.0, v60
	v_add_f32_e32 v65, 1.0, v65
	v_add_f32_e32 v61, 1.0, v61
	v_rcp_f32_e32 v62, v62
	v_rcp_f32_e32 v58, v58
	v_rcp_f32_e32 v63, v63
	v_rcp_f32_e32 v59, v59
	v_rcp_f32_e32 v64, v64
	v_rcp_f32_e32 v60, v60
	v_rcp_f32_e32 v65, v65
	v_rcp_f32_e32 v61, v61
.LBB0_234:
	s_or_b64 exec, exec, s[16:17]
	v_readlane_b32 s16, v252, 3
	v_readlane_b32 s17, v252, 4
	v_add_u32_e32 v68, 0x80, v150
	v_cvt_pk_bf16_f32 v62, v62, v63
	v_cvt_pk_bf16_f32 v63, v64, v65
	v_cvt_pk_bf16_f32 v64, v58, v59
	v_cvt_pk_bf16_f32 v65, v60, v61
	s_nop 0
	v_mov_b64_e32 v[66:67], s[16:17]
	v_mad_i64_i32 v[66:67], s[16:17], v68, s81, v[66:67]
	v_lshl_add_u64 v[66:67], v[142:143], 1, v[66:67]
	global_store_dwordx4 v[66:67], v[62:65], off
	s_and_saveexec_b64 s[16:17], s[14:15]
	s_cbranch_execz .LBB0_236
	s_mov_b32 s7, 0xc1f00000
	v_med3_f32 v54, v54, s7, v233
	v_med3_f32 v50, v50, s7, v233
	v_med3_f32 v55, v55, s7, v233
	v_med3_f32 v51, v51, s7, v233
	v_med3_f32 v56, v56, s7, v233
	v_med3_f32 v52, v52, s7, v233
	v_med3_f32 v57, v57, s7, v233
	v_med3_f32 v53, v53, s7, v233
	v_mul_f32_e32 v54, 0xbfb8aa3b, v54
	v_mul_f32_e32 v50, 0xbfb8aa3b, v50
	v_mul_f32_e32 v55, 0xbfb8aa3b, v55
	v_mul_f32_e32 v51, 0xbfb8aa3b, v51
	v_mul_f32_e32 v56, 0xbfb8aa3b, v56
	v_mul_f32_e32 v52, 0xbfb8aa3b, v52
	v_mul_f32_e32 v57, 0xbfb8aa3b, v57
	v_mul_f32_e32 v53, 0xbfb8aa3b, v53
	v_exp_f32_e32 v54, v54
	v_exp_f32_e32 v50, v50
	v_exp_f32_e32 v55, v55
	v_exp_f32_e32 v51, v51
	v_exp_f32_e32 v56, v56
	v_exp_f32_e32 v52, v52
	v_exp_f32_e32 v57, v57
	v_exp_f32_e32 v53, v53
	v_add_f32_e32 v54, 1.0, v54
	v_add_f32_e32 v50, 1.0, v50
	v_add_f32_e32 v55, 1.0, v55
	v_add_f32_e32 v51, 1.0, v51
	v_add_f32_e32 v56, 1.0, v56
	v_add_f32_e32 v52, 1.0, v52
	v_add_f32_e32 v57, 1.0, v57
	v_add_f32_e32 v53, 1.0, v53
	v_rcp_f32_e32 v54, v54
	v_rcp_f32_e32 v50, v50
	v_rcp_f32_e32 v55, v55
	v_rcp_f32_e32 v51, v51
	v_rcp_f32_e32 v56, v56
	v_rcp_f32_e32 v52, v52
	v_rcp_f32_e32 v57, v57
	v_rcp_f32_e32 v53, v53
.LBB0_236:
	s_or_b64 exec, exec, s[16:17]
	v_cvt_pk_bf16_f32 v54, v54, v55
	v_cvt_pk_bf16_f32 v55, v56, v57
	v_cvt_pk_bf16_f32 v56, v50, v51
	v_cvt_pk_bf16_f32 v57, v52, v53
	global_store_dwordx4 v[66:67], v[54:57], off offset:256
	s_and_saveexec_b64 s[16:17], s[12:13]
	s_cbranch_execz .LBB0_238
	s_mov_b32 s7, 0xc1f00000
	v_med3_f32 v46, v46, s7, v233
	v_med3_f32 v42, v42, s7, v233
	v_med3_f32 v47, v47, s7, v233
	v_med3_f32 v43, v43, s7, v233
	v_med3_f32 v48, v48, s7, v233
	v_med3_f32 v44, v44, s7, v233
	v_med3_f32 v49, v49, s7, v233
	v_med3_f32 v45, v45, s7, v233
	v_mul_f32_e32 v46, 0xbfb8aa3b, v46
	v_mul_f32_e32 v42, 0xbfb8aa3b, v42
	v_mul_f32_e32 v47, 0xbfb8aa3b, v47
	v_mul_f32_e32 v43, 0xbfb8aa3b, v43
	v_mul_f32_e32 v48, 0xbfb8aa3b, v48
	v_mul_f32_e32 v44, 0xbfb8aa3b, v44
	v_mul_f32_e32 v49, 0xbfb8aa3b, v49
	v_mul_f32_e32 v45, 0xbfb8aa3b, v45
	v_exp_f32_e32 v46, v46
	v_exp_f32_e32 v42, v42
	v_exp_f32_e32 v47, v47
	v_exp_f32_e32 v43, v43
	v_exp_f32_e32 v48, v48
	v_exp_f32_e32 v44, v44
	v_exp_f32_e32 v49, v49
	v_exp_f32_e32 v45, v45
	v_add_f32_e32 v46, 1.0, v46
	v_add_f32_e32 v42, 1.0, v42
	v_add_f32_e32 v47, 1.0, v47
	v_add_f32_e32 v43, 1.0, v43
	v_add_f32_e32 v48, 1.0, v48
	v_add_f32_e32 v44, 1.0, v44
	v_add_f32_e32 v49, 1.0, v49
	v_add_f32_e32 v45, 1.0, v45
	v_rcp_f32_e32 v46, v46
	v_rcp_f32_e32 v42, v42
	v_rcp_f32_e32 v47, v47
	v_rcp_f32_e32 v43, v43
	v_rcp_f32_e32 v48, v48
	v_rcp_f32_e32 v44, v44
	v_rcp_f32_e32 v49, v49
	v_rcp_f32_e32 v45, v45
.LBB0_238:
	s_or_b64 exec, exec, s[16:17]
	v_readlane_b32 s16, v252, 3
	v_readlane_b32 s17, v252, 4
	v_add_u32_e32 v52, 0x90, v150
	v_cvt_pk_bf16_f32 v46, v46, v47
	v_cvt_pk_bf16_f32 v47, v48, v49
	v_cvt_pk_bf16_f32 v48, v42, v43
	v_cvt_pk_bf16_f32 v49, v44, v45
	s_nop 0
	v_mov_b64_e32 v[50:51], s[16:17]
	v_mad_i64_i32 v[50:51], s[16:17], v52, s81, v[50:51]
	v_lshl_add_u64 v[50:51], v[142:143], 1, v[50:51]
	global_store_dwordx4 v[50:51], v[46:49], off
	s_and_saveexec_b64 s[16:17], s[14:15]
	s_cbranch_execz .LBB0_240
	s_mov_b32 s7, 0xc1f00000
	v_med3_f32 v38, v38, s7, v233
	v_med3_f32 v34, v34, s7, v233
	v_med3_f32 v39, v39, s7, v233
	v_med3_f32 v35, v35, s7, v233
	v_med3_f32 v40, v40, s7, v233
	v_med3_f32 v36, v36, s7, v233
	v_med3_f32 v41, v41, s7, v233
	v_med3_f32 v37, v37, s7, v233
	v_mul_f32_e32 v38, 0xbfb8aa3b, v38
	v_mul_f32_e32 v34, 0xbfb8aa3b, v34
	v_mul_f32_e32 v39, 0xbfb8aa3b, v39
	v_mul_f32_e32 v35, 0xbfb8aa3b, v35
	v_mul_f32_e32 v40, 0xbfb8aa3b, v40
	v_mul_f32_e32 v36, 0xbfb8aa3b, v36
	v_mul_f32_e32 v41, 0xbfb8aa3b, v41
	v_mul_f32_e32 v37, 0xbfb8aa3b, v37
	v_exp_f32_e32 v38, v38
	v_exp_f32_e32 v34, v34
	v_exp_f32_e32 v39, v39
	v_exp_f32_e32 v35, v35
	v_exp_f32_e32 v40, v40
	v_exp_f32_e32 v36, v36
	v_exp_f32_e32 v41, v41
	v_exp_f32_e32 v37, v37
	v_add_f32_e32 v38, 1.0, v38
	v_add_f32_e32 v34, 1.0, v34
	v_add_f32_e32 v39, 1.0, v39
	v_add_f32_e32 v35, 1.0, v35
	v_add_f32_e32 v40, 1.0, v40
	v_add_f32_e32 v36, 1.0, v36
	v_add_f32_e32 v41, 1.0, v41
	v_add_f32_e32 v37, 1.0, v37
	v_rcp_f32_e32 v38, v38
	v_rcp_f32_e32 v34, v34
	v_rcp_f32_e32 v39, v39
	v_rcp_f32_e32 v35, v35
	v_rcp_f32_e32 v40, v40
	v_rcp_f32_e32 v36, v36
	v_rcp_f32_e32 v41, v41
	v_rcp_f32_e32 v37, v37
.LBB0_240:
	s_or_b64 exec, exec, s[16:17]
	v_cvt_pk_bf16_f32 v38, v38, v39
	v_cvt_pk_bf16_f32 v39, v40, v41
	v_cvt_pk_bf16_f32 v40, v34, v35
	v_cvt_pk_bf16_f32 v41, v36, v37
	global_store_dwordx4 v[50:51], v[38:41], off offset:256
	s_and_saveexec_b64 s[16:17], s[12:13]
	s_cbranch_execz .LBB0_242
	s_mov_b32 s7, 0xc1f00000
	v_med3_f32 v30, v30, s7, v233
	v_med3_f32 v26, v26, s7, v233
	v_med3_f32 v31, v31, s7, v233
	v_med3_f32 v27, v27, s7, v233
	v_med3_f32 v32, v32, s7, v233
	v_med3_f32 v28, v28, s7, v233
	v_med3_f32 v33, v33, s7, v233
	v_med3_f32 v29, v29, s7, v233
	v_mul_f32_e32 v30, 0xbfb8aa3b, v30
	v_mul_f32_e32 v26, 0xbfb8aa3b, v26
	v_mul_f32_e32 v31, 0xbfb8aa3b, v31
	v_mul_f32_e32 v27, 0xbfb8aa3b, v27
	v_mul_f32_e32 v32, 0xbfb8aa3b, v32
	v_mul_f32_e32 v28, 0xbfb8aa3b, v28
	v_mul_f32_e32 v33, 0xbfb8aa3b, v33
	v_mul_f32_e32 v29, 0xbfb8aa3b, v29
	v_exp_f32_e32 v30, v30
	v_exp_f32_e32 v26, v26
	v_exp_f32_e32 v31, v31
	v_exp_f32_e32 v27, v27
	v_exp_f32_e32 v32, v32
	v_exp_f32_e32 v28, v28
	v_exp_f32_e32 v33, v33
	v_exp_f32_e32 v29, v29
	v_add_f32_e32 v30, 1.0, v30
	v_add_f32_e32 v26, 1.0, v26
	v_add_f32_e32 v31, 1.0, v31
	v_add_f32_e32 v27, 1.0, v27
	v_add_f32_e32 v32, 1.0, v32
	v_add_f32_e32 v28, 1.0, v28
	v_add_f32_e32 v33, 1.0, v33
	v_add_f32_e32 v29, 1.0, v29
	v_rcp_f32_e32 v30, v30
	v_rcp_f32_e32 v26, v26
	v_rcp_f32_e32 v31, v31
	v_rcp_f32_e32 v27, v27
	v_rcp_f32_e32 v32, v32
	v_rcp_f32_e32 v28, v28
	v_rcp_f32_e32 v33, v33
	v_rcp_f32_e32 v29, v29
.LBB0_242:
	s_or_b64 exec, exec, s[16:17]
	v_readlane_b32 s16, v252, 3
	v_readlane_b32 s17, v252, 4
	v_add_u32_e32 v36, 0xa0, v150
	v_cvt_pk_bf16_f32 v30, v30, v31
	v_cvt_pk_bf16_f32 v31, v32, v33
	v_cvt_pk_bf16_f32 v32, v26, v27
	v_cvt_pk_bf16_f32 v33, v28, v29
	s_nop 0
	v_mov_b64_e32 v[34:35], s[16:17]
	v_mad_i64_i32 v[34:35], s[16:17], v36, s81, v[34:35]
	v_lshl_add_u64 v[34:35], v[142:143], 1, v[34:35]
	global_store_dwordx4 v[34:35], v[30:33], off
	s_and_saveexec_b64 s[16:17], s[14:15]
	s_cbranch_execz .LBB0_244
	s_mov_b32 s7, 0xc1f00000
	v_med3_f32 v22, v22, s7, v233
	v_med3_f32 v18, v18, s7, v233
	v_med3_f32 v23, v23, s7, v233
	v_med3_f32 v19, v19, s7, v233
	v_med3_f32 v24, v24, s7, v233
	v_med3_f32 v20, v20, s7, v233
	v_med3_f32 v25, v25, s7, v233
	v_med3_f32 v21, v21, s7, v233
	v_mul_f32_e32 v22, 0xbfb8aa3b, v22
	v_mul_f32_e32 v18, 0xbfb8aa3b, v18
	v_mul_f32_e32 v23, 0xbfb8aa3b, v23
	v_mul_f32_e32 v19, 0xbfb8aa3b, v19
	v_mul_f32_e32 v24, 0xbfb8aa3b, v24
	v_mul_f32_e32 v20, 0xbfb8aa3b, v20
	v_mul_f32_e32 v25, 0xbfb8aa3b, v25
	v_mul_f32_e32 v21, 0xbfb8aa3b, v21
	v_exp_f32_e32 v22, v22
	v_exp_f32_e32 v18, v18
	v_exp_f32_e32 v23, v23
	v_exp_f32_e32 v19, v19
	v_exp_f32_e32 v24, v24
	v_exp_f32_e32 v20, v20
	v_exp_f32_e32 v25, v25
	v_exp_f32_e32 v21, v21
	v_add_f32_e32 v22, 1.0, v22
	v_add_f32_e32 v18, 1.0, v18
	v_add_f32_e32 v23, 1.0, v23
	v_add_f32_e32 v19, 1.0, v19
	v_add_f32_e32 v24, 1.0, v24
	v_add_f32_e32 v20, 1.0, v20
	v_add_f32_e32 v25, 1.0, v25
	v_add_f32_e32 v21, 1.0, v21
	v_rcp_f32_e32 v22, v22
	v_rcp_f32_e32 v18, v18
	v_rcp_f32_e32 v23, v23
	v_rcp_f32_e32 v19, v19
	v_rcp_f32_e32 v24, v24
	v_rcp_f32_e32 v20, v20
	v_rcp_f32_e32 v25, v25
	v_rcp_f32_e32 v21, v21
.LBB0_244:
	s_or_b64 exec, exec, s[16:17]
	v_cvt_pk_bf16_f32 v22, v22, v23
	v_cvt_pk_bf16_f32 v23, v24, v25
	v_cvt_pk_bf16_f32 v24, v18, v19
	v_cvt_pk_bf16_f32 v25, v20, v21
	global_store_dwordx4 v[34:35], v[22:25], off offset:256
	s_and_saveexec_b64 s[16:17], s[12:13]
	s_cbranch_execz .LBB0_246
	s_mov_b32 s7, 0xc1f00000
	v_med3_f32 v14, v14, s7, v233
	v_med3_f32 v10, v10, s7, v233
	v_med3_f32 v15, v15, s7, v233
	v_med3_f32 v11, v11, s7, v233
	v_med3_f32 v16, v16, s7, v233
	v_med3_f32 v12, v12, s7, v233
	v_med3_f32 v17, v17, s7, v233
	v_med3_f32 v13, v13, s7, v233
	v_mul_f32_e32 v14, 0xbfb8aa3b, v14
	v_mul_f32_e32 v10, 0xbfb8aa3b, v10
	v_mul_f32_e32 v15, 0xbfb8aa3b, v15
	v_mul_f32_e32 v11, 0xbfb8aa3b, v11
	v_mul_f32_e32 v16, 0xbfb8aa3b, v16
	v_mul_f32_e32 v12, 0xbfb8aa3b, v12
	v_mul_f32_e32 v17, 0xbfb8aa3b, v17
	v_mul_f32_e32 v13, 0xbfb8aa3b, v13
	v_exp_f32_e32 v14, v14
	v_exp_f32_e32 v10, v10
	v_exp_f32_e32 v15, v15
	v_exp_f32_e32 v11, v11
	v_exp_f32_e32 v16, v16
	v_exp_f32_e32 v12, v12
	v_exp_f32_e32 v17, v17
	v_exp_f32_e32 v13, v13
	v_add_f32_e32 v14, 1.0, v14
	v_add_f32_e32 v10, 1.0, v10
	v_add_f32_e32 v15, 1.0, v15
	v_add_f32_e32 v11, 1.0, v11
	v_add_f32_e32 v16, 1.0, v16
	v_add_f32_e32 v12, 1.0, v12
	v_add_f32_e32 v17, 1.0, v17
	v_add_f32_e32 v13, 1.0, v13
	v_rcp_f32_e32 v14, v14
	v_rcp_f32_e32 v10, v10
	v_rcp_f32_e32 v15, v15
	v_rcp_f32_e32 v11, v11
	v_rcp_f32_e32 v16, v16
	v_rcp_f32_e32 v12, v12
	v_rcp_f32_e32 v17, v17
	v_rcp_f32_e32 v13, v13
.LBB0_246:
	s_or_b64 exec, exec, s[16:17]
	v_readlane_b32 s12, v252, 3
	v_readlane_b32 s13, v252, 4
	v_add_u32_e32 v20, 0xb0, v150
	v_cvt_pk_bf16_f32 v14, v14, v15
	v_cvt_pk_bf16_f32 v15, v16, v17
	v_cvt_pk_bf16_f32 v16, v10, v11
	v_cvt_pk_bf16_f32 v17, v12, v13
	s_nop 0
	v_mov_b64_e32 v[18:19], s[12:13]
	v_mad_i64_i32 v[18:19], s[12:13], v20, s81, v[18:19]
	v_lshl_add_u64 v[18:19], v[142:143], 1, v[18:19]
	global_store_dwordx4 v[18:19], v[14:17], off
	s_and_saveexec_b64 s[12:13], s[14:15]
	s_cbranch_execz .LBB0_248
	s_mov_b32 s7, 0xc1f00000
	v_med3_f32 v6, v6, s7, v233
	v_med3_f32 v2, v2, s7, v233
	v_med3_f32 v7, v7, s7, v233
	v_med3_f32 v3, v3, s7, v233
	v_med3_f32 v8, v8, s7, v233
	v_med3_f32 v4, v4, s7, v233
	v_med3_f32 v9, v9, s7, v233
	v_med3_f32 v5, v5, s7, v233
	v_mul_f32_e32 v6, 0xbfb8aa3b, v6
	v_mul_f32_e32 v2, 0xbfb8aa3b, v2
	v_mul_f32_e32 v7, 0xbfb8aa3b, v7
	v_mul_f32_e32 v3, 0xbfb8aa3b, v3
	v_mul_f32_e32 v8, 0xbfb8aa3b, v8
	v_mul_f32_e32 v4, 0xbfb8aa3b, v4
	v_mul_f32_e32 v9, 0xbfb8aa3b, v9
	v_mul_f32_e32 v5, 0xbfb8aa3b, v5
	v_exp_f32_e32 v6, v6
	v_exp_f32_e32 v2, v2
	v_exp_f32_e32 v7, v7
	v_exp_f32_e32 v3, v3
	v_exp_f32_e32 v8, v8
	v_exp_f32_e32 v4, v4
	v_exp_f32_e32 v9, v9
	v_exp_f32_e32 v5, v5
	v_add_f32_e32 v6, 1.0, v6
	v_add_f32_e32 v2, 1.0, v2
	v_add_f32_e32 v7, 1.0, v7
	v_add_f32_e32 v3, 1.0, v3
	v_add_f32_e32 v8, 1.0, v8
	v_add_f32_e32 v4, 1.0, v4
	v_add_f32_e32 v9, 1.0, v9
	v_add_f32_e32 v5, 1.0, v5
	v_rcp_f32_e32 v6, v6
	v_rcp_f32_e32 v2, v2
	v_rcp_f32_e32 v7, v7
	v_rcp_f32_e32 v3, v3
	v_rcp_f32_e32 v8, v8
	v_rcp_f32_e32 v4, v4
	v_rcp_f32_e32 v9, v9
	v_rcp_f32_e32 v5, v5

.LBB0_441:
	ds_read_b128 v[34:37], v169
	ds_read_b128 v[68:71], v169 offset:32
	ds_read_b128 v[72:75], v169 offset:33280
	ds_read_b128 v[76:79], v169 offset:33312
	ds_read_b128 v[80:83], v169 offset:64
	ds_read_b128 v[84:87], v169 offset:96
	ds_read_b128 v[88:91], v169 offset:33344
	ds_read_b128 v[92:95], v169 offset:33376
	s_waitcnt lgkmcnt(7)
	v_mfma_f32_32x32x16_bf16 v[50:65], v[34:37], v[98:101], 0
	s_mov_b32 s0, 0xc1a00000
	s_waitcnt vmcnt(32)
	v_cmp_ngt_f32_e32 vcc, s0, v170
	v_mfma_f32_32x32x16_bf16 v[2:17], v[34:37], v[106:109], 0
	s_waitcnt lgkmcnt(5)
	v_mfma_f32_32x32x16_bf16 v[34:49], v[72:75], v[98:101], 0
	v_mfma_f32_32x32x16_bf16 v[18:33], v[72:75], v[106:109], 0
	v_mfma_f32_32x32x16_bf16 v[50:65], v[68:71], v[102:105], v[50:65]
	v_mfma_f32_32x32x16_bf16 v[2:17], v[68:71], v[110:113], v[2:17]
	v_xor_b32_e32 v68, 0x80000000, v170
	s_waitcnt lgkmcnt(4)
	v_mfma_f32_32x32x16_bf16 v[34:49], v[76:79], v[102:105], v[34:49]
	v_mfma_f32_32x32x16_bf16 v[18:33], v[76:79], v[110:113], v[18:33]
	s_waitcnt lgkmcnt(3)
	v_mfma_f32_32x32x16_bf16 v[50:65], v[80:83], v[114:117], v[50:65]
	v_mfma_f32_32x32x16_bf16 v[2:17], v[80:83], v[122:125], v[2:17]
	s_waitcnt lgkmcnt(1)
	v_mfma_f32_32x32x16_bf16 v[34:49], v[88:91], v[114:117], v[34:49]
	v_mfma_f32_32x32x16_bf16 v[18:33], v[88:91], v[122:125], v[18:33]
	v_mfma_f32_32x32x16_bf16 v[50:65], v[84:87], v[118:121], v[50:65]
	v_mfma_f32_32x32x16_bf16 v[2:17], v[84:87], v[126:129], v[2:17]
	s_waitcnt lgkmcnt(0)
	v_mfma_f32_32x32x16_bf16 v[34:49], v[92:95], v[118:121], v[34:49]
	v_mfma_f32_32x32x16_bf16 v[18:33], v[92:95], v[126:129], v[18:33]
	s_and_saveexec_b64 s[4:5], vcc
	s_cbranch_execz .LBB0_445
	v_mul_f32_e32 v68, 0xbfb8aa3b, v170
	v_rndne_f32_e32 v69, v68
	s_mov_b32 s0, 0xbfb8aa3b
	v_sub_f32_e32 v70, v68, v69
	v_fma_f32 v68, v170, s0, -v68
	v_fmac_f32_e32 v68, 0xb2a5705f, v170
	v_add_f32_e32 v68, v70, v68
	v_exp_f32_e32 v68, v68
	v_cvt_i32_f32_e32 v69, v69
	s_mov_b32 s0, 0x41a00000
	v_cmp_nlt_f32_e32 vcc, s0, v170
	s_mov_b32 s0, 0x42ce8ed0
	v_ldexp_f32 v68, v68, v69
	v_cmp_nlt_f32_e64 s[0:1], s0, v170
	s_nop 1
	v_cndmask_b32_e64 v68, 0, v68, s[0:1]
	s_mov_b32 s0, 0xc2b17218
	v_cmp_ngt_f32_e64 s[0:1], s0, v170
	s_nop 1
	v_cndmask_b32_e64 v68, v234, v68, s[0:1]
	s_and_saveexec_b64 s[0:1], vcc
	s_cbranch_execz .LBB0_444
	v_add_f32_e32 v69, 1.0, v68
	v_add_f32_e32 v70, -1.0, v69
	v_sub_f32_e32 v71, v70, v69
	v_add_f32_e32 v71, 1.0, v71
	v_sub_f32_e32 v70, v68, v70
	v_add_f32_e32 v72, v70, v71
	v_frexp_mant_f32_e32 v73, v69
	v_cvt_f64_f32_e32 v[70:71], v69
	s_mov_b32 s14, 0x3f2aaaab
	v_frexp_exp_i32_f64_e32 v70, v[70:71]
	v_cmp_gt_f32_e32 vcc, s14, v73
	s_mov_b32 s14, 0x3f317218
	s_nop 0
	v_subbrev_co_u32_e32 v78, vcc, 0, v70, vcc
	v_sub_u32_e32 v70, 0, v78
	v_ldexp_f32 v69, v69, v70
	v_ldexp_f32 v70, v72, v70
	v_add_f32_e32 v72, -1.0, v69
	v_add_f32_e32 v71, 1.0, v72
	v_sub_f32_e32 v71, v69, v71
	v_add_f32_e32 v73, v70, v71
	v_add_f32_e32 v71, 1.0, v69
	v_add_f32_e32 v74, -1.0, v71
	v_sub_f32_e32 v69, v69, v74
	v_add_f32_e32 v69, v70, v69
	v_add_f32_e32 v79, v71, v69
	v_rcp_f32_e32 v80, v79
	v_sub_f32_e32 v70, v71, v79
	v_add_f32_e32 v71, v72, v73
	v_add_f32_e32 v69, v69, v70
	v_mul_f32_e32 v82, v71, v80
	v_sub_f32_e32 v70, v72, v71
	v_mul_f32_e32 v72, v79, v82
	v_fma_f32 v74, v82, v79, -v72
	v_fmac_f32_e32 v74, v82, v69
	v_add_f32_e32 v81, v73, v70
	v_add_f32_e32 v70, v72, v74
	v_sub_f32_e32 v73, v71, v70
	v_pk_add_f32 v[76:77], v[70:71], v[72:73] neg_lo:[0,1] neg_hi:[0,1]
	v_mov_b32_e32 v75, v70
	v_pk_add_f32 v[70:71], v[76:77], v[74:75] neg_lo:[0,1] neg_hi:[0,1]
	s_nop 0
	v_add_f32_e32 v71, v81, v71
	v_add_f32_e32 v70, v70, v71
	v_add_f32_e32 v71, v73, v70
	v_mul_f32_e32 v81, v80, v71
	v_mul_f32_e32 v72, v79, v81
	v_fma_f32 v74, v81, v79, -v72
	v_fmac_f32_e32 v74, v81, v69
	v_sub_f32_e32 v69, v73, v71
	v_add_f32_e32 v69, v70, v69
	v_add_f32_e32 v70, v72, v74
	v_sub_f32_e32 v73, v71, v70
	v_pk_add_f32 v[76:77], v[70:71], v[72:73] neg_lo:[0,1] neg_hi:[0,1]
	v_mov_b32_e32 v75, v70
	v_pk_add_f32 v[70:71], v[76:77], v[74:75] neg_lo:[0,1] neg_hi:[0,1]
	s_nop 0
	v_add_f32_e32 v69, v69, v71
	v_add_f32_e32 v69, v70, v69
	v_add_f32_e32 v71, v82, v81
	v_add_f32_e32 v69, v73, v69
	v_sub_f32_e32 v70, v71, v82
	v_mul_f32_e32 v69, v80, v69
	v_sub_f32_e32 v70, v81, v70
	v_add_f32_e32 v69, v70, v69
	v_add_f32_e32 v72, v71, v69
	v_mul_f32_e32 v74, v72, v72
	v_fmamk_f32 v70, v74, 0x3e9b6dac, v227
	v_fmaak_f32 v193, v74, v70, 0x3f2aaada
	v_cvt_f32_i32_e32 v70, v78
	v_sub_f32_e32 v71, v72, v71
	v_sub_f32_e32 v69, v69, v71
	v_mul_f32_e32 v71, v72, v74
	v_pk_mul_f32 v[74:75], v[70:71], v[192:193]
	v_ldexp_f32 v73, v72, 1
	v_fma_f32 v72, v70, s14, -v74
	v_fmac_f32_e32 v72, 0xb102e308, v70
	v_pk_add_f32 v[70:71], v[74:75], v[72:73]
	v_ldexp_f32 v69, v69, 1
	v_sub_f32_e32 v73, v71, v73
	v_sub_f32_e32 v73, v75, v73
	v_add_f32_e32 v77, v69, v73
	v_mov_b32_e32 v76, v74
	v_pk_add_f32 v[74:75], v[70:71], v[74:75] neg_lo:[0,1] neg_hi:[0,1]
	v_pk_add_f32 v[78:79], v[70:71], v[76:77]
	v_mov_b32_e32 v73, v70
	v_mov_b32_e32 v75, v79
	v_pk_add_f32 v[80:81], v[72:73], v[74:75] neg_lo:[0,1] neg_hi:[0,1]
	v_pk_add_f32 v[72:73], v[72:73], v[74:75]
	v_mov_b32_e32 v76, v77
	v_pk_add_f32 v[74:75], v[72:73], v[70:71] op_sel:[1,0] op_sel_hi:[0,1] neg_lo:[0,1] neg_hi:[0,1]
	v_pk_add_f32 v[82:83], v[78:79], v[74:75] op_sel_hi:[1,0] neg_lo:[0,1] neg_hi:[0,1]
	v_mov_b32_e32 v78, v79
	v_mov_b32_e32 v79, v73
	v_pk_mov_b32 v[74:75], v[70:71], v[74:75] op_sel:[1,0]
	v_mov_b32_e32 v77, v70
	v_pk_add_f32 v[74:75], v[78:79], v[74:75] neg_lo:[0,1] neg_hi:[0,1]
	v_mov_b32_e32 v82, v80
	v_pk_add_f32 v[70:71], v[76:77], v[74:75] neg_lo:[0,1] neg_hi:[0,1]
	v_mov_b32_e32 v81, v73
	v_pk_add_f32 v[74:75], v[82:83], v[70:71]
	s_mov_b32 s14, 0x7f800000
	v_pk_add_f32 v[76:77], v[74:75], v[74:75] op_sel:[0,1] op_sel_hi:[1,0]
	v_cmp_neq_f32_e32 vcc, s14, v68
	v_pk_add_f32 v[72:73], v[72:73], v[76:77] op_sel:[1,0] op_sel_hi:[0,1]
	v_mov_b32_e32 v75, v72
	v_pk_add_f32 v[78:79], v[74:75], v[80:81] neg_lo:[0,1] neg_hi:[0,1]
	v_mov_b32_e32 v71, v76
	v_sub_f32_e32 v69, v74, v78
	v_pk_add_f32 v[70:71], v[70:71], v[78:79] neg_lo:[0,1] neg_hi:[0,1]
	v_sub_f32_e32 v69, v80, v69
	v_add_f32_e32 v69, v70, v69
	v_add_f32_e32 v69, v69, v71
	v_add_f32_e32 v69, v72, v69
	s_mov_b32 s14, 0x33800000
	v_cndmask_b32_e32 v69, v234, v69, vcc
	v_cmp_lt_f32_e64 vcc, |v68|, s14
	s_nop 1
	v_cndmask_b32_e32 v68, v69, v68, vcc
